# one static s_setprio 1 for waves 0-3 at kernel entry, every per-segment s_setprio flip deleted (strategy: static priority raise for one wave half)
# speedup vs baseline: 1.0008x; 1.0008x over previous
_Z3fwd4Args:
	v_readfirstlane_b32 s98, v0
	s_nop 3
	s_and_b32 s98, s98, 0x3ff
	s_cmpk_gt_u32 s98, 0xff
	s_cbranch_scc1 .Lstatic_prio_done
	s_setprio 1
.Lstatic_prio_done:
	v_lshl_add_u32 v1, v0, 2, 0
	v_writelane_b32 v251, s2, 0
	s_add_u32 s2, s0, 0xf0
	s_addc_u32 s3, s1, 0
	v_writelane_b32 v251, s2, 1
	v_add_u32_e32 v1, 0x20000, v1
	v_mov_b32_e32 v2, 0
	v_writelane_b32 v251, s3, 2
	s_load_dword s3, s[0:1], 0xf0
	v_readfirstlane_b32 s50, v0
	ds_write2st64_b32 v1, v2, v2 offset1:8
	ds_write2st64_b32 v1, v2, v2 offset0:16 offset1:24
	v_or_b32_e32 v1, 0x800, v0
	s_mov_b64 s[4:5], -1
	s_and_saveexec_b64 s[6:7], s[4:5]
	v_lshl_add_u32 v3, v1, 2, 0
	v_add_u32_e32 v3, 0x20000, v3
	ds_write_b32 v3, v2
	s_or_b64 exec, exec, s[6:7]
	s_and_saveexec_b64 s[6:7], s[4:5]
	s_add_i32 s2, 0, 0x20000
	v_lshl_add_u32 v1, v1, 2, s2
	v_mov_b32_e32 v2, 0
	ds_write_b32 v1, v2 offset:2048
	s_or_b64 exec, exec, s[6:7]
	v_or_b32_e32 v1, 0xc00, v0
	v_cmp_gt_u32_e64 s[4:5], 7, 6
	v_cmp_gt_u32_e64 s[8:9], 7, 5
	s_and_saveexec_b64 s[6:7], s[8:9]
	v_lshl_add_u32 v2, v1, 2, 0
	v_add_u32_e32 v2, 0x20000, v2
	v_mov_b32_e32 v3, 0
	ds_write_b32 v2, v3
	s_or_b64 exec, exec, s[6:7]
	s_and_saveexec_b64 s[6:7], s[4:5]
	s_add_i32 s2, 0, 0x20000
	v_lshl_add_u32 v1, v1, 2, s2
	v_mov_b32_e32 v2, 0
	ds_write_b32 v1, v2 offset:2048
	s_or_b64 exec, exec, s[6:7]
	s_load_dword s2, s[0:1], 0xe0
	s_load_dwordx2 s[4:5], s[0:1], 0xc8
	s_mov_b32 s52, 0
	s_waitcnt lgkmcnt(0)
	s_barrier
	s_cmp_lg_u32 s2, 0
	v_writelane_b32 v251, s4, 3
	s_nop 1
	v_writelane_b32 v251, s5, 4
	s_cselect_b64 s[4:5], -1, 0
	v_writelane_b32 v251, s4, 5
	s_cmp_eq_u32 s2, 0
	s_nop 0
	v_writelane_b32 v251, s5, 6
	s_cbranch_scc1 .LBB0_13
	s_getreg_b32 s2, hwreg(HW_REG_XCC_ID, 0, 4)
	s_and_b32 s51, s2, 15
	v_cmp_eq_u32_e32 vcc, 0, v0
	s_and_saveexec_b64 s[4:5], vcc
	s_cbranch_execz .LBB0_12
	s_mov_b64 s[6:7], exec
	v_mbcnt_lo_u32_b32 v0, s6, 0
	v_mbcnt_hi_u32_b32 v0, s7, v0
	v_cmp_eq_u32_e32 vcc, 0, v0
	s_and_b64 s[8:9], exec, vcc
	s_mov_b64 exec, s[8:9]
	s_cbranch_execz .LBB0_12
	s_load_dwordx2 s[8:9], s[0:1], 0xc8
	s_lshl_b32 s2, s51, 8
	v_mov_b32_e32 v0, 0x4000
	s_waitcnt lgkmcnt(0)
	s_add_u32 s8, s8, s2
	s_addc_u32 s9, s9, 0
	s_bcnt1_i32_b64 s2, s[6:7]
	v_mov_b32_e32 v1, s2
	global_atomic_add v0, v1, s[8:9] offset:1024
